# more C3 per-step trims: negated clamp, direction select as two FMAs, key*decay as one FMA, paired bf16 converts; C1 log2e folded into inputs
# baseline (speedup 1.0000x reference)
; #define LAS __attribute__((address_space(3)))
; __device__ __forceinline__ unsigned cvt_pk_bf16(float lo, float hi) { const bf16x2_t r = __builtin_convertvector((f32x2_t){lo, hi}, bf16x2_t); return __builtin_bit_cast(unsigned, r); }
; __device__ __forceinline__ float fexp(float x) { return __builtin_amdgcn_exp2f(x * 1.4426950408889634f); }
; #define lds lds_hidden(lds0)
; #define DEC WSP(float, W_DEC)
; __device__ __forceinline__ void c1_phase(LAS unsigned char* lds, const bf16_t* __restrict__ LF, const bf16_t* __restrict__ VTH, bf16_t* __restrict__ UT, float* __restrict__ DEC, int first, int count, int stride) {
;     ...
;             float lfv[16], cs[16];
; #pragma unroll
;             for (int i = 0; i < 16; ++i) lfv[i] = __uint_as_float(lfn[i] << 16);
;             if (dir == 0) C1_PF_LF(item, 1); else if (it + 1 < count) C1_PF_LF(item + stride, 0);
;             float run = 0.f;
; #pragma unroll
;             for (int i = 0; i < 16; ++i) { run += lfv[i]; cs[i] = run; }
;             __syncthreads();
;             qtot[tq * 128 + d] = run;
;             __syncthreads();
;             const float q0 = qtot[d], q1 = qtot[128 + d], q2 = qtot[256 + d], q3 = qtot[384 + d];
;             const float pre = (tq > 0 ? q0 : 0.f) + (tq > 1 ? q1 : 0.f) + (tq > 2 ? q2 : 0.f), total = (q0 + q1) + (q2 + q3);
;             unsigned w[8];
; #pragma unroll
;             for (int i = 0; i < 16; i += 2) {
;                 float kd[2];
; #pragma unroll
;                 for (int k = 0; k < 2; ++k) {
;                     const float key = 1.f - fexp(lfv[i + k]);
;                     const float ex = dir == 0 ? (total - (pre + cs[i + k])) : (pre + cs[i + k] - lfv[i + k]);
;                     kd[k] = key * fexp(ex);
;                 }
;                 w[i >> 1] = cvt_pk_bf16(kd[0], kd[1]);
;             }
;             *(LAS u32x4*)(lds + C1_KD + d * R144 + tq * 32) = (u32x4){w[0], w[1], w[2], w[3]};
;             *(LAS u32x4*)(lds + C1_KD + d * R144 + tq * 32 + 16) = (u32x4){w[4], w[5], w[6], w[7]};
;             const size_t idx = ((size_t)(dir * NB + b) * 4 + h) * 32 + j;
;             if (tq == 0) DEC[idx * 128 + d] = fexp(total);
.LBB0_957:
	v_lshlrev_b32_e32 v129, 16, v10
	v_mul_f32_e32 v129, 0x3fb8aa3b, v129
	v_lshlrev_b32_e32 v134, 16, v11
	v_mul_f32_e32 v134, 0x3fb8aa3b, v134
	v_add_f32_e32 v149, 0, v129
	v_lshlrev_b32_e32 v135, 16, v12
	v_mul_f32_e32 v135, 0x3fb8aa3b, v135
	v_add_f32_e32 v150, v149, v134
	v_lshlrev_b32_e32 v136, 16, v13
	v_mul_f32_e32 v136, 0x3fb8aa3b, v136
	v_add_f32_e32 v151, v150, v135
	v_lshlrev_b32_e32 v137, 16, v14
	v_mul_f32_e32 v137, 0x3fb8aa3b, v137
	v_add_f32_e32 v152, v151, v136
	v_lshlrev_b32_e32 v138, 16, v15
	v_mul_f32_e32 v138, 0x3fb8aa3b, v138
	v_add_f32_e32 v153, v152, v137
	v_lshlrev_b32_e32 v139, 16, v16
	v_mul_f32_e32 v139, 0x3fb8aa3b, v139
	v_add_f32_e32 v154, v153, v138
	v_lshlrev_b32_e32 v140, 16, v17
	v_mul_f32_e32 v140, 0x3fb8aa3b, v140
	v_add_f32_e32 v155, v154, v139
	v_exp_f32_e32 v10, v129
	v_exp_f32_e32 v11, v134
	v_lshlrev_b32_e32 v141, 16, v94
	v_mul_f32_e32 v141, 0x3fb8aa3b, v141
	v_add_f32_e32 v156, v155, v140
	v_exp_f32_e32 v12, v135
	v_exp_f32_e32 v13, v136
	v_lshlrev_b32_e32 v142, 16, v95
	v_mul_f32_e32 v142, 0x3fb8aa3b, v142
	v_add_f32_e32 v157, v156, v141
	v_lshlrev_b32_e32 v143, 16, v118
	v_mul_f32_e32 v143, 0x3fb8aa3b, v143
	v_add_f32_e32 v158, v157, v142
	v_lshlrev_b32_e32 v144, 16, v119
	v_mul_f32_e32 v144, 0x3fb8aa3b, v144
	v_add_f32_e32 v159, v158, v143
	v_pk_add_f32 v[16:17], v[10:11], 1.0 op_sel_hi:[1,0] neg_lo:[1,0] neg_hi:[1,0]
	v_lshlrev_b32_e32 v145, 16, v120
	v_mul_f32_e32 v145, 0x3fb8aa3b, v145
	v_add_f32_e32 v160, v159, v144
	v_pk_add_f32 v[94:95], v[12:13], 1.0 op_sel_hi:[1,0] neg_lo:[1,0] neg_hi:[1,0]
	v_exp_f32_e32 v10, v139
	v_exp_f32_e32 v11, v140
	v_lshlrev_b32_e32 v146, 16, v121
	v_mul_f32_e32 v146, 0x3fb8aa3b, v146
	v_add_f32_e32 v161, v160, v145
	v_exp_f32_e32 v12, v141
	v_exp_f32_e32 v13, v142
	v_lshlrev_b32_e32 v147, 16, v122
	v_mul_f32_e32 v147, 0x3fb8aa3b, v147
	v_add_f32_e32 v162, v161, v146
	v_exp_f32_e32 v118, v143
	v_exp_f32_e32 v119, v144
	v_lshlrev_b32_e32 v148, 16, v123
	v_mul_f32_e32 v148, 0x3fb8aa3b, v148
	v_add_f32_e32 v163, v162, v147
	v_pk_add_f32 v[122:123], v[10:11], 1.0 op_sel_hi:[1,0] neg_lo:[1,0] neg_hi:[1,0]
	v_add_f32_e32 v11, v163, v148
	s_waitcnt lgkmcnt(0)
	s_barrier
	v_pk_add_f32 v[124:125], v[12:13], 1.0 op_sel_hi:[1,0] neg_lo:[1,0] neg_hi:[1,0]
	ds_write_b32 v96, v11 offset:36864
	s_waitcnt lgkmcnt(0)
	s_barrier
	ds_read2st64_b32 v[12:13], v97 offset0:144 offset1:146
	v_pk_add_f32 v[126:127], v[118:119], 1.0 op_sel_hi:[1,0] neg_lo:[1,0] neg_hi:[1,0]
	ds_read2st64_b32 v[118:119], v97 offset0:148 offset1:150
	v_exp_f32_e32 v128, v147
	s_waitcnt lgkmcnt(1)
	v_cndmask_b32_e64 v10, 0, v12, s[4:5]
	v_cndmask_b32_e64 v130, 0, v13, s[6:7]
	v_add_f32_e32 v131, v10, v130
	s_waitcnt lgkmcnt(0)
	v_cndmask_b32_e64 v133, 0, v118, s[8:9]
	v_mov_b32_e32 v130, v118
	v_mov_b32_e32 v132, v119
	v_add_f32_e32 v10, v12, v13
	v_pk_add_f32 v[130:131], v[130:131], v[132:133]
	v_add_f32_e32 v12, v149, v131
	v_pk_add_f32 v[10:11], v[10:11], v[130:131]
	v_sub_f32_e32 v13, v10, v12
	v_sub_f32_e32 v12, v12, v129
	v_cndmask_b32_e64 v12, v12, v13, s[14:15]
	v_add_f32_e32 v13, v150, v131
	v_sub_f32_e32 v118, v10, v13
	v_sub_f32_e32 v13, v13, v134
	v_cndmask_b32_e64 v13, v13, v118, s[14:15]
	v_add_f32_e32 v118, v151, v131
	v_sub_f32_e32 v119, v10, v118
	v_sub_f32_e32 v118, v118, v135
	v_cndmask_b32_e64 v118, v118, v119, s[14:15]
	v_add_f32_e32 v119, v152, v131
	v_sub_f32_e32 v129, v10, v119
	v_sub_f32_e32 v119, v119, v136
	v_exp_f32_e32 v12, v12
	v_exp_f32_e32 v13, v13
	v_cndmask_b32_e64 v119, v119, v129, s[14:15]
	v_exp_f32_e32 v118, v118
	v_exp_f32_e32 v119, v119
	v_pk_mul_f32 v[12:13], v[16:17], v[12:13]
	v_exp_f32_e32 v14, v137
	v_cvt_pk_bf16_f32 v12, v12, v13
	v_add_f32_e32 v13, v153, v131
	v_pk_mul_f32 v[16:17], v[94:95], v[118:119]
	v_sub_f32_e32 v94, v10, v13
	v_sub_f32_e32 v13, v13, v137
	v_cndmask_b32_e64 v13, v13, v94, s[14:15]
	v_exp_f32_e32 v94, v13
	v_add_f32_e32 v13, v154, v131
	v_sub_f32_e32 v95, v10, v13
	v_sub_f32_e32 v13, v13, v138
	v_cndmask_b32_e64 v13, v13, v95, s[14:15]
	v_exp_f32_e32 v15, v138
	v_exp_f32_e32 v95, v13
	v_add_f32_e32 v13, v155, v131
	v_pk_add_f32 v[14:15], v[14:15], 1.0 op_sel_hi:[1,0] neg_lo:[1,0] neg_hi:[1,0]
	v_sub_f32_e32 v118, v10, v13
	v_sub_f32_e32 v13, v13, v139
	v_cndmask_b32_e64 v13, v13, v118, s[14:15]
	v_pk_mul_f32 v[14:15], v[14:15], v[94:95]
	v_cvt_pk_bf16_f32 v14, v14, v15
	v_add_f32_e32 v15, v157, v131
	v_exp_f32_e32 v118, v13
	v_add_f32_e32 v13, v156, v131
	v_sub_f32_e32 v94, v10, v15
	v_sub_f32_e32 v15, v15, v141
	v_sub_f32_e32 v119, v10, v13
	v_sub_f32_e32 v13, v13, v140
	v_cndmask_b32_e64 v15, v15, v94, s[14:15]
	v_cndmask_b32_e64 v13, v13, v119, s[14:15]
	v_exp_f32_e32 v94, v15
	v_add_f32_e32 v15, v158, v131
	v_exp_f32_e32 v119, v13
	v_sub_f32_e32 v95, v10, v15
	v_sub_f32_e32 v15, v15, v142
	v_cndmask_b32_e64 v15, v15, v95, s[14:15]
	v_exp_f32_e32 v95, v15
	v_add_f32_e32 v15, v159, v131
	v_cvt_pk_bf16_f32 v13, v16, v17
	v_pk_mul_f32 v[16:17], v[122:123], v[118:119]
	v_sub_f32_e32 v118, v10, v15
	v_sub_f32_e32 v15, v15, v143
	v_cndmask_b32_e64 v15, v15, v118, s[14:15]
	v_exp_f32_e32 v122, v15
	v_add_f32_e32 v15, v160, v131
	v_sub_f32_e32 v118, v10, v15
	v_sub_f32_e32 v15, v15, v144
	v_cndmask_b32_e64 v15, v15, v118, s[14:15]
	v_exp_f32_e32 v123, v15
	v_cvt_pk_bf16_f32 v15, v16, v17
	v_pk_mul_f32 v[16:17], v[124:125], v[94:95]
	v_cvt_pk_bf16_f32 v118, v16, v17
	v_pk_mul_f32 v[16:17], v[126:127], v[122:123]
	v_cvt_pk_bf16_f32 v119, v16, v17
	v_add_f32_e32 v16, v161, v131
	v_sub_f32_e32 v17, v10, v16
	v_sub_f32_e32 v16, v16, v145
	v_cndmask_b32_e64 v16, v16, v17, s[14:15]
	v_add_f32_e32 v17, v162, v131
	v_sub_f32_e32 v94, v10, v17
	v_sub_f32_e32 v17, v17, v146
	v_cndmask_b32_e64 v17, v17, v94, s[14:15]
	v_add_f32_e32 v94, v163, v131
	v_sub_f32_e32 v95, v10, v94
	v_sub_f32_e32 v94, v94, v147
	v_exp_f32_e32 v120, v145
	v_exp_f32_e32 v121, v146
	v_cndmask_b32_e64 v94, v94, v95, s[14:15]
	v_sub_f32_e32 v95, v10, v11
	v_sub_f32_e32 v11, v11, v148
	v_exp_f32_e32 v16, v16
	v_exp_f32_e32 v17, v17
	v_cndmask_b32_e64 v11, v11, v95, s[14:15]
	v_exp_f32_e32 v129, v148
	v_exp_f32_e32 v94, v94
	v_exp_f32_e32 v95, v11
	v_pk_add_f32 v[120:121], v[120:121], 1.0 op_sel_hi:[1,0] neg_lo:[1,0] neg_hi:[1,0]
	s_add_i32 s14, s3, s2
	v_pk_mul_f32 v[16:17], v[120:121], v[16:17]
	s_ashr_i32 s15, s14, 31
	v_cvt_pk_bf16_f32 v120, v16, v17
	v_pk_add_f32 v[16:17], v[128:129], 1.0 op_sel_hi:[1,0] neg_lo:[1,0] neg_hi:[1,0]
	s_lshl_b64 s[14:15], s[14:15], 7
	v_pk_mul_f32 v[16:17], v[16:17], v[94:95]
	s_or_b64 s[14:15], s[14:15], s[90:91]
	v_cvt_pk_bf16_f32 v121, v16, v17
	ds_write_b128 v99, v[12:15]
	ds_write_b128 v99, v[118:121] offset:16
	s_and_saveexec_b64 s[16:17], s[10:11]
	s_cbranch_execz .LBB0_950
	v_exp_f32_e32 v12, v10
	s_lshl_b64 s[20:21], s[14:15], 9
	v_lshl_add_u64 v[10:11], v[26:27], 0, s[20:21]
	global_store_dword v[10:11], v12, off
	s_branch .LBB0_950

; #define LAS __attribute__((address_space(3)))
; __device__ __forceinline__ bf16_t f2bf(float f) { unsigned u = __float_as_uint(f); u += 0x7FFFu + ((u >> 16) & 1u); return (bf16_t)(u >> 16); }
; __device__ __forceinline__ float fexp(float x) { return __builtin_amdgcn_exp2f(x * 1.4426950408889634f); }
; #define lds lds_hidden(lds0)
; __device__ __forceinline__ void c3_phase(LAS unsigned char* lds, const bf16_t* __restrict__ QH, const bf16_t* __restrict__ LF, const bf16_t* __restrict__ VTH, const bf16_t* __restrict__ SIN, ...
;     ...
;             const float q0 = qtot[d], q1 = qtot[128 + d], q2 = qtot[256 + d], q3 = qtot[384 + d];
;             const float pre = (tq > 0 ? q0 : 0.f) + (tq > 1 ? q1 : 0.f) + (tq > 2 ? q2 : 0.f), total = (q0 + q1) + (q2 + q3);
;             const float mref = dir == 0 ? (q0 + q1) : (q2 + q3);
; #pragma unroll
;             for (int i = 0; i < 16; ++i) {
;                 const int t = tq * 16 + i;
;                 const float bt = dir == 0 ? (pre + cs[i]) : (total - (pre + cs[i]) + lfv[i]);
;                 const float q = qv[i];
;                 const float key = 1.f - fexp(lfv[i]);
;                 *(LAS bf16_t*)(lds + C3_QT + t * R272 + d * 2) = f2bf(q * fexp(bt));
;                 *(LAS bf16_t*)(lds + C3_QH + t * R272 + d * 2) = f2bf(q * fexp(fminf(bt - mref, 80.f)));
;                 *(LAS bf16_t*)(lds + C3_KH + t * R272 + d * 2) = f2bf(key * fexp(fminf(mref - bt, 80.f)));
;             }
.LBB0_1097:
	s_waitcnt vmcnt(19)
	v_lshlrev_b32_e32 v215, 16, v162
	v_mul_f32_e32 v215, 0x3fb8aa3b, v215
	s_waitcnt vmcnt(18)
	v_lshlrev_b32_e32 v220, 16, v164
	v_mul_f32_e32 v220, 0x3fb8aa3b, v220
	v_add_f32_e32 v224, 0, v215
	s_waitcnt vmcnt(17)
	v_lshlrev_b32_e32 v221, 16, v65
	v_mul_f32_e32 v221, 0x3fb8aa3b, v221
	v_add_f32_e32 v225, v224, v220
	s_waitcnt vmcnt(16)
	v_lshlrev_b32_e32 v222, 16, v166
	v_mul_f32_e32 v222, 0x3fb8aa3b, v222
	v_add_f32_e32 v226, v225, v221
	s_waitcnt vmcnt(15)
	v_lshlrev_b32_e32 v223, 16, v160
	v_mul_f32_e32 v223, 0x3fb8aa3b, v223
	v_add_f32_e32 v227, v226, v222
	s_waitcnt vmcnt(14)
	v_lshlrev_b32_e32 v213, 16, v161
	v_mul_f32_e32 v213, 0x3fb8aa3b, v213
	v_add_f32_e32 v228, v227, v223
	s_waitcnt vmcnt(13)
	v_lshlrev_b32_e32 v211, 16, v163
	v_mul_f32_e32 v211, 0x3fb8aa3b, v211
	v_add_f32_e32 v214, v228, v213
	s_waitcnt vmcnt(12)
	v_lshlrev_b32_e32 v209, 16, v169
	v_mul_f32_e32 v209, 0x3fb8aa3b, v209
	v_add_f32_e32 v212, v214, v211
	s_waitcnt vmcnt(11)
	v_lshlrev_b32_e32 v207, 16, v165
	v_mul_f32_e32 v207, 0x3fb8aa3b, v207
	v_add_f32_e32 v210, v212, v209
	s_waitcnt vmcnt(10)
	v_lshlrev_b32_e32 v51, 16, v167
	v_mul_f32_e32 v51, 0x3fb8aa3b, v51
	v_add_f32_e32 v208, v210, v207
	s_waitcnt vmcnt(9)
	v_lshlrev_b32_e32 v49, 16, v168
	v_mul_f32_e32 v49, 0x3fb8aa3b, v49
	v_add_f32_e32 v206, v208, v51
	s_waitcnt vmcnt(8)
	v_lshlrev_b32_e32 v47, 16, v172
	v_mul_f32_e32 v47, 0x3fb8aa3b, v47
	v_add_f32_e32 v50, v206, v49
	s_waitcnt vmcnt(7)
	v_lshlrev_b32_e32 v45, 16, v170
	v_mul_f32_e32 v45, 0x3fb8aa3b, v45
	v_add_f32_e32 v48, v50, v47
	s_waitcnt vmcnt(6)
	v_lshlrev_b32_e32 v43, 16, v171
	v_mul_f32_e32 v43, 0x3fb8aa3b, v43
	v_add_f32_e32 v46, v48, v45
	s_waitcnt vmcnt(5)
	v_lshlrev_b32_e32 v41, 16, v173
	v_mul_f32_e32 v41, 0x3fb8aa3b, v41
	v_add_f32_e32 v44, v46, v43
	s_waitcnt vmcnt(4)
	v_lshlrev_b32_e32 v37, 16, v174
	v_mul_f32_e32 v37, 0x3fb8aa3b, v37
	v_add_f32_e32 v42, v44, v41
	v_add_f32_e32 v38, v42, v37
	s_waitcnt lgkmcnt(0)
	s_barrier
	ds_write_b32 v175, v38
	s_waitcnt vmcnt(3)
	ds_write_b128 v181, v[2:5]
	s_waitcnt vmcnt(2)
	ds_write_b128 v182, v[6:9]
	s_waitcnt vmcnt(1)
	ds_write_b128 v183, v[10:13]
	s_waitcnt vmcnt(0)
	ds_write_b128 v184, v[14:17]
	s_waitcnt lgkmcnt(0)
	s_barrier
	ds_read2st64_b32 v[216:217], v176 offset1:2
	ds_read2st64_b32 v[218:219], v176 offset0:4 offset1:6
	s_xor_b64 s[78:79], s[2:3], -1
	s_and_b64 vcc, exec, s[78:79]
	s_mov_b64 s[92:93], -1
	s_waitcnt lgkmcnt(1)
	v_cndmask_b32_e64 v36, 0, v216, s[4:5]
	v_cndmask_b32_e64 v39, 0, v217, s[6:7]
	v_add_f32_e32 v36, v36, v39
	s_waitcnt lgkmcnt(0)
	v_cndmask_b32_e64 v39, 0, v218, s[8:9]
	v_add_f32_e32 v39, v36, v39
	v_add_f32_e32 v36, v216, v217
	v_add_f32_e32 v216, v218, v219
	v_add_f32_e32 v40, v36, v216
	v_cndmask_b32_e64 v231, -1.0, 1.0, s[2:3]
	v_cndmask_b32_e64 v232, v40, 0, s[2:3]
	v_cndmask_b32_e64 v233, 1.0, 0, s[2:3]
	v_cndmask_b32_e64 v36, v216, v36, s[2:3]
	v_add_f32_e32 v216, v224, v39
	v_fma_f32 v217, v231, v216, v232
	v_fma_f32 v216, v233, v215, v217
	v_exp_f32_e32 v217, v216
	v_exp_f32_e32 v215, v215
	v_add_f32_e32 v214, v214, v39
	v_mul_f32_e32 v234, v217, v190
	v_sub_f32_e32 v217, v216, v36
	v_max_f32_e32 v216, 0xc2e6d4ca, v217
	v_exp_f32_e64 v216, -v216
	v_min_f32_e32 v217, 0x42e6d4ca, v217
	v_exp_f32_e32 v217, v217
	v_fma_f32 v215, -v215, v216, v216
	v_cvt_pk_bf16_f32 v215, v215, v215
	ds_write_b16 v185, v215 offset:34816
	v_add_f32_e32 v215, v225, v39
	v_mul_f32_e32 v217, v217, v190
	v_fma_f32 v216, v231, v215, v232
	v_cvt_pk_bf16_f32 v217, v234, v217
	v_fma_f32 v215, v233, v220, v216
	ds_write_b16 v185, v217
	ds_write_b16_d16_hi v185, v217 offset:17408
	v_exp_f32_e32 v217, v215
	v_exp_f32_e32 v216, v220
	v_add_f32_e32 v212, v212, v39
	v_mul_f32_e32 v235, v217, v191
	v_sub_f32_e32 v217, v215, v36
	v_max_f32_e32 v215, 0xc2e6d4ca, v217
	v_exp_f32_e64 v215, -v215
	v_min_f32_e32 v217, 0x42e6d4ca, v217
	v_exp_f32_e32 v217, v217
	v_fma_f32 v215, -v216, v215, v215
	v_cvt_pk_bf16_f32 v215, v215, v215
	ds_write_b16 v185, v215 offset:35088
	v_add_f32_e32 v215, v226, v39
	v_mul_f32_e32 v217, v217, v191
	v_fma_f32 v216, v231, v215, v232
	v_cvt_pk_bf16_f32 v217, v235, v217
	v_fma_f32 v215, v233, v221, v216
	ds_write_b16 v185, v217 offset:272
	ds_write_b16_d16_hi v185, v217 offset:17680
	v_exp_f32_e32 v217, v215
	v_exp_f32_e32 v216, v221
	v_add_f32_e32 v210, v210, v39
	v_mul_f32_e32 v236, v217, v192
	v_sub_f32_e32 v217, v215, v36
	v_max_f32_e32 v215, 0xc2e6d4ca, v217
	v_exp_f32_e64 v215, -v215
	v_min_f32_e32 v217, 0x42e6d4ca, v217
	v_exp_f32_e32 v217, v217
	v_fma_f32 v215, -v216, v215, v215
	v_cvt_pk_bf16_f32 v215, v215, v215
	ds_write_b16 v185, v215 offset:35360
	v_add_f32_e32 v215, v227, v39
	v_mul_f32_e32 v217, v217, v192
	v_fma_f32 v216, v231, v215, v232
	v_cvt_pk_bf16_f32 v217, v236, v217
	v_fma_f32 v215, v233, v222, v216
	ds_write_b16 v185, v217 offset:544
	ds_write_b16_d16_hi v185, v217 offset:17952
	v_exp_f32_e32 v217, v215
	v_exp_f32_e32 v216, v222
	v_add_f32_e32 v208, v208, v39
	v_mul_f32_e32 v237, v217, v193
	v_sub_f32_e32 v217, v215, v36
	v_max_f32_e32 v215, 0xc2e6d4ca, v217
	v_exp_f32_e64 v215, -v215
	v_min_f32_e32 v217, 0x42e6d4ca, v217
	v_exp_f32_e32 v217, v217
	v_fma_f32 v215, -v216, v215, v215
	v_cvt_pk_bf16_f32 v215, v215, v215
	ds_write_b16 v185, v215 offset:35632
	v_add_f32_e32 v215, v228, v39
	v_mul_f32_e32 v217, v217, v193
	v_fma_f32 v216, v231, v215, v232
	v_cvt_pk_bf16_f32 v217, v237, v217
	v_fma_f32 v215, v233, v223, v216
	ds_write_b16 v185, v217 offset:816
	ds_write_b16_d16_hi v185, v217 offset:18224
	v_exp_f32_e32 v217, v215
	v_exp_f32_e32 v216, v223
	v_add_f32_e32 v206, v206, v39
	v_mul_f32_e32 v238, v217, v194
; #define LAS __attribute__((address_space(3)))
; __device__ __forceinline__ bf16_t f2bf(float f) { unsigned u = __float_as_uint(f); u += 0x7FFFu + ((u >> 16) & 1u); return (bf16_t)(u >> 16); }
; __device__ __forceinline__ float fexp(float x) { return __builtin_amdgcn_exp2f(x * 1.4426950408889634f); }
; #define lds lds_hidden(lds0)
; __device__ __forceinline__ void c3_phase(LAS unsigned char* lds, const bf16_t* __restrict__ QH, const bf16_t* __restrict__ LF, const bf16_t* __restrict__ VTH, const bf16_t* __restrict__ SIN, ...
;     ...
; #pragma unroll
;             for (int i = 0; i < 16; ++i) {
;                 const int t = tq * 16 + i;
;                 const float bt = dir == 0 ? (pre + cs[i]) : (total - (pre + cs[i]) + lfv[i]);
;                 const float q = qv[i];
;                 const float key = 1.f - fexp(lfv[i]);
;                 *(LAS bf16_t*)(lds + C3_QT + t * R272 + d * 2) = f2bf(q * fexp(bt));
;                 *(LAS bf16_t*)(lds + C3_QH + t * R272 + d * 2) = f2bf(q * fexp(fminf(bt - mref, 80.f)));
;                 *(LAS bf16_t*)(lds + C3_KH + t * R272 + d * 2) = f2bf(key * fexp(fminf(mref - bt, 80.f)));
;             }
	v_sub_f32_e32 v217, v215, v36
	v_max_f32_e32 v215, 0xc2e6d4ca, v217
	v_exp_f32_e64 v215, -v215
	v_add_f32_e32 v50, v50, v39
	v_add_f32_e32 v48, v48, v39
	v_fma_f32 v215, -v216, v215, v215
	v_cvt_pk_bf16_f32 v215, v215, v215
	ds_write_b16 v185, v215 offset:35904
	v_fma_f32 v215, v231, v214, v232
	v_fma_f32 v214, v233, v213, v215
	v_exp_f32_e32 v215, v214
	v_exp_f32_e32 v213, v213
	v_add_f32_e32 v46, v46, v39
	v_mul_f32_e32 v239, v215, v195
	v_sub_f32_e32 v215, v214, v36
	v_max_f32_e32 v214, 0xc2e6d4ca, v215
	v_exp_f32_e64 v214, -v214
	v_add_f32_e32 v44, v44, v39
	v_add_f32_e32 v42, v42, v39
	v_fma_f32 v213, -v213, v214, v214
	v_cvt_pk_bf16_f32 v213, v213, v213
	ds_write_b16 v185, v213 offset:36176
	v_fma_f32 v213, v231, v212, v232
	v_fma_f32 v212, v233, v211, v213
	v_exp_f32_e32 v213, v212
	v_exp_f32_e32 v211, v211
	v_add_f32_e32 v38, v38, v39
	v_mul_f32_e32 v240, v213, v196
	v_sub_f32_e32 v213, v212, v36
	v_max_f32_e32 v212, 0xc2e6d4ca, v213
	v_exp_f32_e64 v212, -v212
	v_fma_f32 v39, v231, v38, v232
	v_fma_f32 v211, -v211, v212, v212
	v_cvt_pk_bf16_f32 v211, v211, v211
	ds_write_b16 v185, v211 offset:36448
	v_fma_f32 v211, v231, v210, v232
	v_fma_f32 v210, v233, v209, v211
	v_exp_f32_e32 v211, v210
	v_exp_f32_e32 v209, v209
	v_fma_f32 v38, v233, v37, v39
	v_mul_f32_e32 v241, v211, v197
	v_sub_f32_e32 v211, v210, v36
	v_max_f32_e32 v210, 0xc2e6d4ca, v211
	v_exp_f32_e64 v210, -v210
	v_exp_f32_e32 v39, v38
	v_fma_f32 v209, -v209, v210, v210
	v_cvt_pk_bf16_f32 v209, v209, v209
	ds_write_b16 v185, v209 offset:36720
	v_fma_f32 v209, v231, v208, v232
	v_fma_f32 v208, v233, v207, v209
	v_exp_f32_e32 v209, v208
	v_exp_f32_e32 v207, v207
	v_mul_f32_e32 v39, v39, v205
	v_mul_f32_e32 v242, v209, v198
	v_sub_f32_e32 v209, v208, v36
	v_max_f32_e32 v208, 0xc2e6d4ca, v209
	v_exp_f32_e64 v208, -v208
	v_min_f32_e32 v217, 0x42e6d4ca, v217
	v_min_f32_e32 v215, 0x42e6d4ca, v215
	v_fma_f32 v207, -v207, v208, v208
	v_cvt_pk_bf16_f32 v207, v207, v207
	ds_write_b16 v185, v207 offset:36992
	v_fma_f32 v207, v231, v206, v232
	v_fma_f32 v206, v233, v51, v207
	v_exp_f32_e32 v207, v206
	v_exp_f32_e32 v51, v51
	v_min_f32_e32 v213, 0x42e6d4ca, v213
	v_mul_f32_e32 v243, v207, v199
	v_sub_f32_e32 v207, v206, v36
	v_max_f32_e32 v206, 0xc2e6d4ca, v207
	v_exp_f32_e64 v206, -v206
	v_min_f32_e32 v211, 0x42e6d4ca, v211
	v_min_f32_e32 v209, 0x42e6d4ca, v209
	v_fma_f32 v51, -v51, v206, v206
	v_cvt_pk_bf16_f32 v51, v51, v51
	ds_write_b16 v185, v51 offset:37264
	v_fma_f32 v51, v231, v50, v232
	v_fma_f32 v50, v233, v49, v51
	v_exp_f32_e32 v51, v50
	v_exp_f32_e32 v49, v49
	v_min_f32_e32 v207, 0x42e6d4ca, v207
	v_mul_f32_e32 v244, v51, v200
	v_sub_f32_e32 v51, v50, v36
	v_max_f32_e32 v50, 0xc2e6d4ca, v51
	v_exp_f32_e64 v50, -v50
	v_min_f32_e32 v51, 0x42e6d4ca, v51
	v_fma_f32 v49, -v49, v50, v50
	v_cvt_pk_bf16_f32 v49, v49, v49
	ds_write_b16 v185, v49 offset:37536
	v_fma_f32 v49, v231, v48, v232
	v_fma_f32 v48, v233, v47, v49
	v_exp_f32_e32 v49, v48
	v_exp_f32_e32 v47, v47
	v_mul_f32_e32 v245, v49, v201
	v_sub_f32_e32 v49, v48, v36
	v_max_f32_e32 v48, 0xc2e6d4ca, v49
	v_exp_f32_e64 v48, -v48
	v_min_f32_e32 v49, 0x42e6d4ca, v49
	v_fma_f32 v47, -v47, v48, v48
	v_cvt_pk_bf16_f32 v47, v47, v47
	ds_write_b16 v185, v47 offset:37808
	v_fma_f32 v47, v231, v46, v232
	v_fma_f32 v46, v233, v45, v47
	v_exp_f32_e32 v47, v46
	v_exp_f32_e32 v45, v45
	v_mul_f32_e32 v246, v47, v202
	v_sub_f32_e32 v47, v46, v36
	v_max_f32_e32 v46, 0xc2e6d4ca, v47
	v_exp_f32_e64 v46, -v46
	v_min_f32_e32 v47, 0x42e6d4ca, v47
	v_fma_f32 v45, -v45, v46, v46
	v_cvt_pk_bf16_f32 v45, v45, v45
	ds_write_b16 v185, v45 offset:38080
	v_fma_f32 v45, v231, v44, v232
	v_fma_f32 v44, v233, v43, v45
	v_exp_f32_e32 v45, v44
	v_exp_f32_e32 v43, v43
	v_mul_f32_e32 v247, v45, v203
	v_sub_f32_e32 v45, v44, v36
	v_max_f32_e32 v44, 0xc2e6d4ca, v45
	v_exp_f32_e64 v44, -v44
	v_min_f32_e32 v45, 0x42e6d4ca, v45
	v_fma_f32 v43, -v43, v44, v44
	v_cvt_pk_bf16_f32 v43, v43, v43
	ds_write_b16 v185, v43 offset:38352
	v_fma_f32 v43, v231, v42, v232
	v_fma_f32 v42, v233, v41, v43
	v_exp_f32_e32 v43, v42
	v_cvt_pk_bf16_f32 v39, v39, v39
	ds_write_b16 v185, v39 offset:4080
	v_mul_f32_e32 v248, v43, v204
	v_sub_f32_e32 v43, v42, v36
	v_max_f32_e32 v42, 0xc2e6d4ca, v43
	v_sub_f32_e32 v39, v38, v36
	v_max_f32_e32 v36, 0xc2e6d4ca, v39
	v_min_f32_e32 v43, 0x42e6d4ca, v43
	v_min_f32_e32 v39, 0x42e6d4ca, v39
	v_exp_f32_e32 v41, v41
	v_exp_f32_e32 v37, v37
	v_exp_f32_e32 v217, v217
	v_exp_f32_e32 v215, v215
	v_exp_f32_e32 v213, v213
	v_exp_f32_e32 v211, v211
	v_exp_f32_e32 v209, v209
	v_exp_f32_e32 v207, v207
	v_exp_f32_e32 v51, v51
	v_exp_f32_e32 v49, v49
	v_exp_f32_e32 v47, v47
	v_exp_f32_e32 v45, v45
	v_exp_f32_e32 v43, v43
	v_exp_f32_e64 v42, -v42
	v_exp_f32_e32 v39, v39
	v_exp_f32_e64 v36, -v36
	v_mul_f32_e32 v217, v217, v194
	v_mul_f32_e32 v215, v215, v195
	v_mul_f32_e32 v213, v213, v196
	v_mul_f32_e32 v211, v211, v197
	v_mul_f32_e32 v209, v209, v198
	v_mul_f32_e32 v207, v207, v199
	v_mul_f32_e32 v51, v51, v200
	v_mul_f32_e32 v49, v49, v201
	v_mul_f32_e32 v47, v47, v202
	v_mul_f32_e32 v45, v45, v203
	v_mul_f32_e32 v43, v43, v204
	v_fma_f32 v41, -v41, v42, v42
	v_mul_f32_e32 v39, v39, v205
	v_fma_f32 v36, -v37, v36, v36
	v_cvt_pk_bf16_f32 v217, v238, v217
	v_cvt_pk_bf16_f32 v215, v239, v215
	v_cvt_pk_bf16_f32 v213, v240, v213
	v_cvt_pk_bf16_f32 v211, v241, v211
	v_cvt_pk_bf16_f32 v209, v242, v209
	v_cvt_pk_bf16_f32 v207, v243, v207
	v_cvt_pk_bf16_f32 v51, v244, v51
	v_cvt_pk_bf16_f32 v49, v245, v49
	v_cvt_pk_bf16_f32 v47, v246, v47
	v_cvt_pk_bf16_f32 v45, v247, v45
	v_cvt_pk_bf16_f32 v43, v248, v43
	v_cvt_pk_bf16_f32 v41, v41, v41
	v_cvt_pk_bf16_f32 v39, v39, v39
	v_cvt_pk_bf16_f32 v36, v36, v36
	ds_write_b16 v185, v217 offset:1088
	ds_write_b16_d16_hi v185, v217 offset:18496
	ds_write_b16 v185, v215 offset:1360
	ds_write_b16_d16_hi v185, v215 offset:18768
	ds_write_b16 v185, v213 offset:1632
	ds_write_b16_d16_hi v185, v213 offset:19040
	ds_write_b16 v185, v211 offset:1904
	ds_write_b16_d16_hi v185, v211 offset:19312
	ds_write_b16 v185, v209 offset:2176
	ds_write_b16_d16_hi v185, v209 offset:19584
	ds_write_b16 v185, v207 offset:2448
	ds_write_b16_d16_hi v185, v207 offset:19856
	ds_write_b16 v185, v51 offset:2720
	ds_write_b16_d16_hi v185, v51 offset:20128
	ds_write_b16 v185, v49 offset:2992
	ds_write_b16_d16_hi v185, v49 offset:20400
	ds_write_b16 v185, v47 offset:3264
	ds_write_b16_d16_hi v185, v47 offset:20672
	ds_write_b16 v185, v45 offset:3536
	ds_write_b16_d16_hi v185, v45 offset:20944
	ds_write_b16 v185, v43 offset:3808
	ds_write_b16_d16_hi v185, v43 offset:21216
	ds_write_b16 v185, v41 offset:38624
	ds_write_b16 v185, v39 offset:21488
	ds_write_b16 v185, v36 offset:38896
	s_waitcnt lgkmcnt(0)
	s_barrier
; __device__ __forceinline__ void c3_phase(LAS unsigned char* lds, const bf16_t* __restrict__ QH, const bf16_t* __restrict__ LF, const bf16_t* __restrict__ VTH, const bf16_t* __restrict__ SIN, ...
;     ...
;             if (dir == 0) C3_PREFETCH(item, 1); else if (item + G < NB * 4 * 32) C3_PREFETCH(item + G, 0);
	s_cbranch_vccz .LBB0_1101
	s_andn2_b64 vcc, exec, s[86:87]
	s_cbranch_vccnz .LBB0_1100
	global_load_ushort v162, v[82:83], off
	global_load_ushort v164, v[82:83], off offset:2048
	global_load_ushort v65, v[84:85], off
	global_load_ushort v166, v[86:87], off
	global_load_ushort v160, v[88:89], off
	global_load_ushort v161, v[90:91], off
	global_load_ushort v163, v[92:93], off
	global_load_ushort v169, v[94:95], off
	global_load_ushort v165, v[96:97], off
	global_load_ushort v167, v[98:99], off
	global_load_ushort v168, v[100:101], off
	global_load_ushort v172, v[102:103], off
	global_load_ushort v170, v[104:105], off
	global_load_ushort v171, v[106:107], off
	global_load_ushort v173, v[108:109], off
	global_load_ushort v174, v[110:111], off
	global_load_dwordx4 v[2:5], v[112:113], off nt
	global_load_dwordx4 v[6:9], v[114:115], off nt
	global_load_dwordx4 v[10:13], v[116:117], off nt
	global_load_dwordx4 v[14:17], v[118:119], off nt
